# GEMM LDS-DMA loads with sc1 (L1 bypass; the DMA data is never reused from the vector L1)
# speedup vs baseline: 1.0088x; 1.0088x over previous
_Z8gemm_qkvPKDF16_S0_PKfPDF16_S3_S3_Pj:
	v_readfirstlane_b32 s13, v0
	s_lshr_b32 s8, s13, 6
	v_bfe_u32 v2, v0, 3, 3
	s_load_dwordx4 s[4:7], s[0:1], 0x0
	v_lshl_or_b32 v6, s8, 3, v2
	v_lshrrev_b32_e32 v2, 1, v6
	s_mul_i32 s16, s3, 0xc0
	v_xor_b32_e32 v4, v2, v0
	v_add_u32_e32 v2, s16, v6
	v_ashrrev_i32_e32 v3, 31, v2
	s_bfe_u32 s15, s13, 0x20006
	v_lshlrev_b64 v[2:3], 11, v[2:3]
	v_lshlrev_b32_e32 v4, 4, v4
	s_mul_i32 s10, s2, 0xc0
	s_mul_i32 s2, s15, 48
	s_waitcnt lgkmcnt(0)
	v_lshl_add_u64 v[2:3], s[4:5], 0, v[2:3]
	v_and_b32_e32 v4, 0x70, v4
	v_mov_b32_e32 v5, 0
	s_add_i32 s17, s2, s10
	v_lshl_add_u64 v[218:219], v[2:3], 0, v[4:5]
	v_add_u32_e32 v2, s10, v6
	s_lshl_b32 s8, s8, 10
	v_ashrrev_i32_e32 v3, 31, v2
	s_cmp_lg_u32 0x400, -1
	v_lshlrev_b64 v[2:3], 11, v[2:3]
	s_cselect_b32 s4, 0x400, 0
	v_lshl_add_u64 v[2:3], s[6:7], 0, v[2:3]
	s_add_i32 s11, s8, s4
	s_mov_b32 s4, m0
	s_mov_b32 m0, s11
	s_nop 0
	global_load_lds_dwordx4 v[218:219], off sc1
	s_mov_b32 m0, s4
	v_lshl_add_u64 v[220:221], v[2:3], 0, v[4:5]
	s_add_i32 s4, s11, 0x6000
	s_mov_b32 s5, m0
	s_mov_b32 m0, s4
	s_nop 0
	global_load_lds_dwordx4 v[220:221], off sc1
	s_mov_b32 m0, s5
	s_mov_b64 s[4:5], 0x20000
	v_lshl_add_u64 v[222:223], v[218:219], 0, s[4:5]
	s_add_i32 s9, s11, 0x2000
	s_mov_b32 s6, m0
	s_mov_b32 m0, s9
	s_nop 0
	global_load_lds_dwordx4 v[222:223], off sc1
	s_mov_b32 m0, s6
	v_lshl_add_u64 v[224:225], v[220:221], 0, s[4:5]
	s_add_i32 s4, s11, 0x8000
	s_mov_b32 s5, m0
	s_mov_b32 m0, s4
	s_nop 0
	global_load_lds_dwordx4 v[224:225], off sc1
	s_mov_b32 m0, s5
	s_mov_b64 s[4:5], 0x40000
	v_lshl_add_u64 v[226:227], v[218:219], 0, s[4:5]
	s_add_i32 s12, s11, 0x4000
	s_mov_b32 s6, m0
	s_mov_b32 m0, s12
	s_nop 0
	global_load_lds_dwordx4 v[226:227], off sc1
	s_mov_b32 m0, s6
	v_lshl_add_u64 v[228:229], v[220:221], 0, s[4:5]
	s_add_i32 s4, s11, 0xa000
	s_mov_b32 s5, m0
	s_mov_b32 m0, s4
	s_nop 0
	global_load_lds_dwordx4 v[228:229], off sc1
	s_mov_b32 m0, s5
	s_cmpk_gt_i32 s17, 0x7d0
	s_cselect_b64 s[4:5], -1, 0
	s_lshr_b32 s14, s13, 8
	s_mul_i32 s6, s14, 0x3000
	s_add_i32 s13, s6, 0x400
	s_mov_b64 s[6:7], 0x80
	s_add_i32 s18, s11, 0xc000
	v_lshl_add_u64 v[2:3], v[218:219], 0, s[6:7]
	s_mov_b32 s30, m0
	s_mov_b32 m0, s18
	s_nop 0
	global_load_lds_dwordx4 v[2:3], off sc1
	s_mov_b32 m0, s30
	s_add_i32 s19, s11, 0x12000
	v_lshl_add_u64 v[2:3], v[220:221], 0, s[6:7]
	s_mov_b32 s6, m0
	s_mov_b32 m0, s19
	s_nop 0
	global_load_lds_dwordx4 v[2:3], off sc1
	s_mov_b32 m0, s6
	s_mov_b64 s[6:7], 0x20080
	s_add_i32 s20, s11, 0xe000
	v_lshl_add_u64 v[2:3], v[218:219], 0, s[6:7]
	s_mov_b32 s18, m0
	s_mov_b32 m0, s20
	s_nop 0
	global_load_lds_dwordx4 v[2:3], off sc1
	s_mov_b32 m0, s18
	s_add_i32 s21, s11, 0x14000
	v_lshl_add_u64 v[2:3], v[220:221], 0, s[6:7]
	s_mov_b32 s6, m0
	s_mov_b32 m0, s21
	s_nop 0
	global_load_lds_dwordx4 v[2:3], off sc1
	s_mov_b32 m0, s6
	s_mov_b64 s[6:7], 0x40080
	v_lshl_add_u64 v[2:3], v[218:219], 0, s[6:7]
	s_add_i32 s22, s11, 0x10000
	s_mov_b32 s18, m0
	s_mov_b32 m0, s22
	s_nop 0
	global_load_lds_dwordx4 v[2:3], off sc1
	s_mov_b32 m0, s18
	v_lshl_add_u64 v[2:3], v[220:221], 0, s[6:7]
	v_and_b32_e32 v1, 15, v0
	v_bfe_u32 v231, v0, 4, 2
	s_add_i32 s23, s11, 0x16000
	s_mov_b32 s6, m0
	s_mov_b32 m0, s23
	s_nop 0
	global_load_lds_dwordx4 v[2:3], off sc1
	s_mov_b32 m0, s6
	v_lshrrev_b32_e32 v3, 1, v0
	v_lshlrev_b32_e32 v2, 7, v1
	v_bfe_u32 v4, v0, 1, 3
	v_bitop3_b32 v3, v231, v3, 7 bitop3:0x78
	v_lshl_or_b32 v238, v3, 4, v2
	v_bitop3_b32 v3, v231, v4, 4 bitop3:0x36
	v_lshl_or_b32 v240, v3, 4, v2
	s_mulk_i32 s15, 0x1800
	s_addk_i32 s15, 0x6400
	v_add_u32_e32 v158, s13, v238
	v_add_u32_e32 v160, s13, v240
	v_add_u32_e32 v162, s15, v238
	v_add_u32_e32 v164, s15, v240
	s_add_u32 m0, s11, 0x17f00
	s_nop 0
	global_load_lds_dwordx4 v[218:219], off offset:256 sc1
	s_add_u32 m0, s11, 0x19f00
	s_nop 0
	global_load_lds_dwordx4 v[222:223], off offset:256 sc1
	s_add_u32 m0, s11, 0x1bf00
	s_nop 0
	global_load_lds_dwordx4 v[226:227], off offset:256 sc1
	s_load_dwordx2 s[24:25], s[0:1], 0x10
	s_mov_b32 s20, 0x180
	s_mov_b32 s21, 0
	v_lshl_add_u64 v[218:219], v[218:219], 0, s[20:21]
	v_lshl_add_u64 v[222:223], v[222:223], 0, s[20:21]
	v_lshl_add_u64 v[226:227], v[226:227], 0, s[20:21]
	v_lshl_add_u64 v[220:221], v[220:221], 0, s[20:21]
	v_lshl_add_u64 v[224:225], v[224:225], 0, s[20:21]
	v_lshl_add_u64 v[228:229], v[228:229], 0, s[20:21]
	v_add_u32_e32 v159, 0x18000, v158
	v_add_u32_e32 v161, 0x18000, v160
	v_add_u32_e32 v163, 0x18000, v162
	v_add_u32_e32 v165, 0x18000, v164
	v_mov_b32_e32 v82, 0
	v_mov_b32_e32 v83, 0
	v_mov_b32_e32 v84, 0
	v_mov_b32_e32 v85, 0
	v_mov_b32_e32 v58, 0
	v_mov_b32_e32 v59, 0
	v_mov_b32_e32 v60, 0
	v_mov_b32_e32 v61, 0
	v_mov_b32_e32 v14, 0
	v_mov_b32_e32 v15, 0
	v_mov_b32_e32 v16, 0
	v_mov_b32_e32 v17, 0
	v_mov_b32_e32 v78, 0
	v_mov_b32_e32 v79, 0
	v_mov_b32_e32 v80, 0
	v_mov_b32_e32 v81, 0
	v_mov_b32_e32 v22, 0
	v_mov_b32_e32 v23, 0
	v_mov_b32_e32 v24, 0
	v_mov_b32_e32 v25, 0
	v_mov_b32_e32 v30, 0
	v_mov_b32_e32 v31, 0
	v_mov_b32_e32 v32, 0
	v_mov_b32_e32 v33, 0
	v_mov_b32_e32 v74, 0
	v_mov_b32_e32 v75, 0
	v_mov_b32_e32 v76, 0
	v_mov_b32_e32 v77, 0
	v_mov_b32_e32 v18, 0
	v_mov_b32_e32 v19, 0
	v_mov_b32_e32 v20, 0
	v_mov_b32_e32 v21, 0
	v_mov_b32_e32 v26, 0
	v_mov_b32_e32 v27, 0
	v_mov_b32_e32 v28, 0
	v_mov_b32_e32 v29, 0
	v_mov_b32_e32 v70, 0
	v_mov_b32_e32 v71, 0
	v_mov_b32_e32 v72, 0
	v_mov_b32_e32 v73, 0
	v_mov_b32_e32 v46, 0
	v_mov_b32_e32 v47, 0
	v_mov_b32_e32 v48, 0
	v_mov_b32_e32 v49, 0
	v_mov_b32_e32 v240, 0
	v_mov_b32_e32 v241, 0
	v_mov_b32_e32 v242, 0
	v_mov_b32_e32 v243, 0
	v_mov_b32_e32 v66, 0
	v_mov_b32_e32 v67, 0
	v_mov_b32_e32 v68, 0
	v_mov_b32_e32 v69, 0
	v_mov_b32_e32 v42, 0
	v_mov_b32_e32 v43, 0
	v_mov_b32_e32 v44, 0
	v_mov_b32_e32 v45, 0
	v_mov_b32_e32 v236, 0
	v_mov_b32_e32 v237, 0
	v_mov_b32_e32 v238, 0
	v_mov_b32_e32 v239, 0
	v_mov_b32_e32 v62, 0
	v_mov_b32_e32 v63, 0
	v_mov_b32_e32 v64, 0
	v_mov_b32_e32 v65, 0
	v_mov_b32_e32 v38, 0
	v_mov_b32_e32 v39, 0
	v_mov_b32_e32 v40, 0
	v_mov_b32_e32 v41, 0
	v_mov_b32_e32 v34, 0
	v_mov_b32_e32 v35, 0
	v_mov_b32_e32 v36, 0
	v_mov_b32_e32 v37, 0
	s_not_b64 s[6:7], s[4:5]
	s_mov_b32 s22, 4
	s_waitcnt vmcnt(9) lgkmcnt(0)
	s_barrier
	ds_read_b128 v[134:137], v162
	ds_read_b128 v[138:141], v162 offset:2048
	ds_read_b128 v[142:145], v162 offset:4096
	ds_read_b128 v[86:89], v158
	ds_read_b128 v[90:93], v158 offset:2048
	ds_read_b128 v[94:97], v158 offset:4096
	ds_read_b128 v[98:101], v158 offset:6144
	ds_read_b128 v[102:105], v158 offset:8192
	ds_read_b128 v[106:109], v158 offset:10240
	ds_read_b128 v[110:113], v160
	ds_read_b128 v[114:117], v160 offset:2048
	ds_read_b128 v[118:121], v160 offset:4096
	ds_read_b128 v[122:125], v160 offset:6144
	ds_read_b128 v[126:129], v160 offset:8192
	ds_read_b128 v[130:133], v160 offset:10240
	ds_read_b128 v[146:149], v164
	ds_read_b128 v[150:153], v164 offset:2048
	ds_read_b128 v[154:157], v164 offset:4096
	s_and_b64 vcc, exec, s[4:5]
	s_cbranch_vccnz .Lgemm_N_loop
.Lgemm_T_loop:
	s_waitcnt lgkmcnt(9)
	s_add_u32 m0, s11, 0x1e080
	v_mfma_f32_16x16x32_f16 v[82:85], v[134:137], v[86:89], v[82:85]
	global_load_lds_dwordx4 v[220:221], off offset:-128 sc1
	v_mfma_f32_16x16x32_f16 v[58:61], v[138:141], v[86:89], v[58:61]
	v_mfma_f32_16x16x32_f16 v[14:17], v[142:145], v[86:89], v[14:17]
	v_mfma_f32_16x16x32_f16 v[78:81], v[134:137], v[90:93], v[78:81]
	v_mfma_f32_16x16x32_f16 v[22:25], v[138:141], v[90:93], v[22:25]
	v_mfma_f32_16x16x32_f16 v[30:33], v[142:145], v[90:93], v[30:33]
	s_add_u32 m0, s11, 0x20080
	v_mfma_f32_16x16x32_f16 v[74:77], v[134:137], v[94:97], v[74:77]
	global_load_lds_dwordx4 v[224:225], off offset:-128 sc1
	v_mfma_f32_16x16x32_f16 v[18:21], v[138:141], v[94:97], v[18:21]
	v_mfma_f32_16x16x32_f16 v[26:29], v[142:145], v[94:97], v[26:29]
	v_mfma_f32_16x16x32_f16 v[70:73], v[134:137], v[98:101], v[70:73]
	v_mfma_f32_16x16x32_f16 v[46:49], v[138:141], v[98:101], v[46:49]
	v_mfma_f32_16x16x32_f16 v[240:243], v[142:145], v[98:101], v[240:243]
	s_add_u32 m0, s11, 0x22080
	v_mfma_f32_16x16x32_f16 v[66:69], v[134:137], v[102:105], v[66:69]
	global_load_lds_dwordx4 v[228:229], off offset:-128 sc1
	v_mfma_f32_16x16x32_f16 v[42:45], v[138:141], v[102:105], v[42:45]
	v_mfma_f32_16x16x32_f16 v[236:239], v[142:145], v[102:105], v[236:239]
	v_mfma_f32_16x16x32_f16 v[62:65], v[134:137], v[106:109], v[62:65]
	v_mfma_f32_16x16x32_f16 v[38:41], v[138:141], v[106:109], v[38:41]
	v_mfma_f32_16x16x32_f16 v[34:37], v[142:145], v[106:109], v[34:37]
	s_waitcnt vmcnt(6) lgkmcnt(0)
	s_barrier
	s_add_u32 m0, s11, 0x0
	ds_read_b128 v[134:137], v162 offset:49152
	global_load_lds_dwordx4 v[218:219], off sc1
	v_mfma_f32_16x16x32_f16 v[82:85], v[146:149], v[110:113], v[82:85]
	ds_read_b128 v[138:141], v162 offset:51200
	v_mfma_f32_16x16x32_f16 v[58:61], v[150:153], v[110:113], v[58:61]
	ds_read_b128 v[142:145], v162 offset:53248
	v_mfma_f32_16x16x32_f16 v[14:17], v[154:157], v[110:113], v[14:17]
	ds_read_b128 v[86:89], v158 offset:49152
	v_mfma_f32_16x16x32_f16 v[78:81], v[146:149], v[114:117], v[78:81]
	ds_read_b128 v[90:93], v158 offset:51200
	v_mfma_f32_16x16x32_f16 v[22:25], v[150:153], v[114:117], v[22:25]
	ds_read_b128 v[94:97], v158 offset:53248
	v_mfma_f32_16x16x32_f16 v[30:33], v[154:157], v[114:117], v[30:33]
	s_add_u32 m0, s11, 0x2000
	ds_read_b128 v[98:101], v158 offset:55296
	global_load_lds_dwordx4 v[222:223], off sc1
	v_mfma_f32_16x16x32_f16 v[74:77], v[146:149], v[118:121], v[74:77]
	ds_read_b128 v[102:105], v158 offset:57344
	v_mfma_f32_16x16x32_f16 v[18:21], v[150:153], v[118:121], v[18:21]
	ds_read_b128 v[106:109], v158 offset:59392
	v_mfma_f32_16x16x32_f16 v[26:29], v[154:157], v[118:121], v[26:29]
	ds_read_b128 v[110:113], v160 offset:49152
	v_mfma_f32_16x16x32_f16 v[70:73], v[146:149], v[122:125], v[70:73]
	ds_read_b128 v[114:117], v160 offset:51200
	v_mfma_f32_16x16x32_f16 v[46:49], v[150:153], v[122:125], v[46:49]
	v_mfma_f32_16x16x32_f16 v[240:243], v[154:157], v[122:125], v[240:243]
	s_add_u32 m0, s11, 0x4000
	ds_read_b128 v[118:121], v160 offset:53248
	global_load_lds_dwordx4 v[226:227], off sc1
	v_mfma_f32_16x16x32_f16 v[66:69], v[146:149], v[126:129], v[66:69]
	ds_read_b128 v[122:125], v160 offset:55296
	v_mfma_f32_16x16x32_f16 v[42:45], v[150:153], v[126:129], v[42:45]
	v_mfma_f32_16x16x32_f16 v[236:239], v[154:157], v[126:129], v[236:239]
	ds_read_b128 v[126:129], v160 offset:57344
	v_mfma_f32_16x16x32_f16 v[62:65], v[146:149], v[130:133], v[62:65]
	v_mfma_f32_16x16x32_f16 v[38:41], v[150:153], v[130:133], v[38:41]
	v_mfma_f32_16x16x32_f16 v[34:37], v[154:157], v[130:133], v[34:37]
	ds_read_b128 v[130:133], v160 offset:59392
	ds_read_b128 v[146:149], v164 offset:49152
	ds_read_b128 v[150:153], v164 offset:51200
	ds_read_b128 v[154:157], v164 offset:53248
	s_waitcnt lgkmcnt(9)
	s_add_u32 m0, s11, 0x6000
	v_mfma_f32_16x16x32_f16 v[82:85], v[134:137], v[86:89], v[82:85]
	global_load_lds_dwordx4 v[220:221], off sc1
	v_mfma_f32_16x16x32_f16 v[58:61], v[138:141], v[86:89], v[58:61]
	v_mfma_f32_16x16x32_f16 v[14:17], v[142:145], v[86:89], v[14:17]
	v_mfma_f32_16x16x32_f16 v[78:81], v[134:137], v[90:93], v[78:81]
	v_mfma_f32_16x16x32_f16 v[22:25], v[138:141], v[90:93], v[22:25]
	v_mfma_f32_16x16x32_f16 v[30:33], v[142:145], v[90:93], v[30:33]
	s_add_u32 m0, s11, 0x8000
	v_mfma_f32_16x16x32_f16 v[74:77], v[134:137], v[94:97], v[74:77]
	global_load_lds_dwordx4 v[224:225], off sc1
	v_mfma_f32_16x16x32_f16 v[18:21], v[138:141], v[94:97], v[18:21]
	v_mfma_f32_16x16x32_f16 v[26:29], v[142:145], v[94:97], v[26:29]
	v_mfma_f32_16x16x32_f16 v[70:73], v[134:137], v[98:101], v[70:73]
	v_mfma_f32_16x16x32_f16 v[46:49], v[138:141], v[98:101], v[46:49]
	v_mfma_f32_16x16x32_f16 v[240:243], v[142:145], v[98:101], v[240:243]
	s_add_u32 m0, s11, 0xa000
	v_mfma_f32_16x16x32_f16 v[66:69], v[134:137], v[102:105], v[66:69]
	global_load_lds_dwordx4 v[228:229], off sc1
	v_mfma_f32_16x16x32_f16 v[42:45], v[138:141], v[102:105], v[42:45]
	v_mfma_f32_16x16x32_f16 v[236:239], v[142:145], v[102:105], v[236:239]
	v_mfma_f32_16x16x32_f16 v[62:65], v[134:137], v[106:109], v[62:65]
	v_mfma_f32_16x16x32_f16 v[38:41], v[138:141], v[106:109], v[38:41]
	v_mfma_f32_16x16x32_f16 v[34:37], v[142:145], v[106:109], v[34:37]
	s_waitcnt vmcnt(6) lgkmcnt(0)
	s_barrier
	s_add_u32 m0, s11, 0xbf80
	ds_read_b128 v[134:137], v163
	global_load_lds_dwordx4 v[218:219], off offset:128 sc1
	v_mfma_f32_16x16x32_f16 v[82:85], v[146:149], v[110:113], v[82:85]
	ds_read_b128 v[138:141], v163 offset:2048
	v_mfma_f32_16x16x32_f16 v[58:61], v[150:153], v[110:113], v[58:61]
	ds_read_b128 v[142:145], v163 offset:4096
	v_mfma_f32_16x16x32_f16 v[14:17], v[154:157], v[110:113], v[14:17]
	ds_read_b128 v[86:89], v159
	v_mfma_f32_16x16x32_f16 v[78:81], v[146:149], v[114:117], v[78:81]
	ds_read_b128 v[90:93], v159 offset:2048
	v_mfma_f32_16x16x32_f16 v[22:25], v[150:153], v[114:117], v[22:25]
	ds_read_b128 v[94:97], v159 offset:4096
	v_mfma_f32_16x16x32_f16 v[30:33], v[154:157], v[114:117], v[30:33]
	s_add_u32 m0, s11, 0xdf80
	ds_read_b128 v[98:101], v159 offset:6144
	global_load_lds_dwordx4 v[222:223], off offset:128 sc1
	v_mfma_f32_16x16x32_f16 v[74:77], v[146:149], v[118:121], v[74:77]
	ds_read_b128 v[102:105], v159 offset:8192
	v_mfma_f32_16x16x32_f16 v[18:21], v[150:153], v[118:121], v[18:21]
	ds_read_b128 v[106:109], v159 offset:10240
	v_mfma_f32_16x16x32_f16 v[26:29], v[154:157], v[118:121], v[26:29]
	ds_read_b128 v[110:113], v161
	v_mfma_f32_16x16x32_f16 v[70:73], v[146:149], v[122:125], v[70:73]
	ds_read_b128 v[114:117], v161 offset:2048
	v_mfma_f32_16x16x32_f16 v[46:49], v[150:153], v[122:125], v[46:49]
	v_mfma_f32_16x16x32_f16 v[240:243], v[154:157], v[122:125], v[240:243]
	s_add_u32 m0, s11, 0xff80
	ds_read_b128 v[118:121], v161 offset:4096
	global_load_lds_dwordx4 v[226:227], off offset:128 sc1
	v_mfma_f32_16x16x32_f16 v[66:69], v[146:149], v[126:129], v[66:69]
	ds_read_b128 v[122:125], v161 offset:6144
	v_mfma_f32_16x16x32_f16 v[42:45], v[150:153], v[126:129], v[42:45]
	v_mfma_f32_16x16x32_f16 v[236:239], v[154:157], v[126:129], v[236:239]
	ds_read_b128 v[126:129], v161 offset:8192
	v_mfma_f32_16x16x32_f16 v[62:65], v[146:149], v[130:133], v[62:65]
	v_mfma_f32_16x16x32_f16 v[38:41], v[150:153], v[130:133], v[38:41]
	v_mfma_f32_16x16x32_f16 v[34:37], v[154:157], v[130:133], v[34:37]
	ds_read_b128 v[130:133], v161 offset:10240
	ds_read_b128 v[146:149], v165
	ds_read_b128 v[150:153], v165 offset:2048
	ds_read_b128 v[154:157], v165 offset:4096
	s_waitcnt lgkmcnt(9)
	s_add_u32 m0, s11, 0x11f80
	v_mfma_f32_16x16x32_f16 v[82:85], v[134:137], v[86:89], v[82:85]
	global_load_lds_dwordx4 v[220:221], off offset:128 sc1
	v_mfma_f32_16x16x32_f16 v[58:61], v[138:141], v[86:89], v[58:61]
	v_mfma_f32_16x16x32_f16 v[14:17], v[142:145], v[86:89], v[14:17]
	v_mfma_f32_16x16x32_f16 v[78:81], v[134:137], v[90:93], v[78:81]
	v_mfma_f32_16x16x32_f16 v[22:25], v[138:141], v[90:93], v[22:25]
	v_mfma_f32_16x16x32_f16 v[30:33], v[142:145], v[90:93], v[30:33]
	s_add_u32 m0, s11, 0x13f80
	v_mfma_f32_16x16x32_f16 v[74:77], v[134:137], v[94:97], v[74:77]
	global_load_lds_dwordx4 v[224:225], off offset:128 sc1
	v_mfma_f32_16x16x32_f16 v[18:21], v[138:141], v[94:97], v[18:21]
	v_mfma_f32_16x16x32_f16 v[26:29], v[142:145], v[94:97], v[26:29]
	v_mfma_f32_16x16x32_f16 v[70:73], v[134:137], v[98:101], v[70:73]
	v_mfma_f32_16x16x32_f16 v[46:49], v[138:141], v[98:101], v[46:49]
	v_mfma_f32_16x16x32_f16 v[240:243], v[142:145], v[98:101], v[240:243]
	s_add_u32 m0, s11, 0x15f80
	v_mfma_f32_16x16x32_f16 v[66:69], v[134:137], v[102:105], v[66:69]
	global_load_lds_dwordx4 v[228:229], off offset:128 sc1
	v_mfma_f32_16x16x32_f16 v[42:45], v[138:141], v[102:105], v[42:45]
	v_mfma_f32_16x16x32_f16 v[236:239], v[142:145], v[102:105], v[236:239]
	v_mfma_f32_16x16x32_f16 v[62:65], v[134:137], v[106:109], v[62:65]
	v_mfma_f32_16x16x32_f16 v[38:41], v[138:141], v[106:109], v[38:41]
	v_mfma_f32_16x16x32_f16 v[34:37], v[142:145], v[106:109], v[34:37]
	s_waitcnt vmcnt(6) lgkmcnt(0)
	s_barrier
	s_add_u32 m0, s11, 0x17f00
	ds_read_b128 v[134:137], v162
	global_load_lds_dwordx4 v[218:219], off offset:256 sc1
	v_mfma_f32_16x16x32_f16 v[82:85], v[146:149], v[110:113], v[82:85]
	ds_read_b128 v[138:141], v162 offset:2048
	v_mfma_f32_16x16x32_f16 v[58:61], v[150:153], v[110:113], v[58:61]
	ds_read_b128 v[142:145], v162 offset:4096
	v_mfma_f32_16x16x32_f16 v[14:17], v[154:157], v[110:113], v[14:17]
	ds_read_b128 v[86:89], v158
	v_mfma_f32_16x16x32_f16 v[78:81], v[146:149], v[114:117], v[78:81]
	ds_read_b128 v[90:93], v158 offset:2048
	v_mfma_f32_16x16x32_f16 v[22:25], v[150:153], v[114:117], v[22:25]
	ds_read_b128 v[94:97], v158 offset:4096
	v_mfma_f32_16x16x32_f16 v[30:33], v[154:157], v[114:117], v[30:33]
	s_add_u32 m0, s11, 0x19f00
	ds_read_b128 v[98:101], v158 offset:6144
	global_load_lds_dwordx4 v[222:223], off offset:256 sc1
	v_mfma_f32_16x16x32_f16 v[74:77], v[146:149], v[118:121], v[74:77]
	ds_read_b128 v[102:105], v158 offset:8192
	v_mfma_f32_16x16x32_f16 v[18:21], v[150:153], v[118:121], v[18:21]
	ds_read_b128 v[106:109], v158 offset:10240
	v_mfma_f32_16x16x32_f16 v[26:29], v[154:157], v[118:121], v[26:29]
	ds_read_b128 v[110:113], v160
	v_mfma_f32_16x16x32_f16 v[70:73], v[146:149], v[122:125], v[70:73]
	ds_read_b128 v[114:117], v160 offset:2048
	v_mfma_f32_16x16x32_f16 v[46:49], v[150:153], v[122:125], v[46:49]
	v_mfma_f32_16x16x32_f16 v[240:243], v[154:157], v[122:125], v[240:243]
	s_add_u32 m0, s11, 0x1bf00
	ds_read_b128 v[118:121], v160 offset:4096
	global_load_lds_dwordx4 v[226:227], off offset:256 sc1
	v_mfma_f32_16x16x32_f16 v[66:69], v[146:149], v[126:129], v[66:69]
	ds_read_b128 v[122:125], v160 offset:6144
	v_mfma_f32_16x16x32_f16 v[42:45], v[150:153], v[126:129], v[42:45]
	v_mfma_f32_16x16x32_f16 v[236:239], v[154:157], v[126:129], v[236:239]
	ds_read_b128 v[126:129], v160 offset:8192
	v_mfma_f32_16x16x32_f16 v[62:65], v[146:149], v[130:133], v[62:65]
	v_mfma_f32_16x16x32_f16 v[38:41], v[150:153], v[130:133], v[38:41]
	v_mfma_f32_16x16x32_f16 v[34:37], v[154:157], v[130:133], v[34:37]
	ds_read_b128 v[130:133], v160 offset:10240
	ds_read_b128 v[146:149], v164
	ds_read_b128 v[150:153], v164 offset:2048
	ds_read_b128 v[154:157], v164 offset:4096
	v_lshl_add_u64 v[218:219], v[218:219], 0, s[20:21]
	v_lshl_add_u64 v[222:223], v[222:223], 0, s[20:21]
	v_lshl_add_u64 v[226:227], v[226:227], 0, s[20:21]
	v_lshl_add_u64 v[220:221], v[220:221], 0, s[20:21]
	v_lshl_add_u64 v[224:225], v[224:225], 0, s[20:21]
	v_lshl_add_u64 v[228:229], v[228:229], 0, s[20:21]
	s_sub_u32 s22, s22, 1
	s_cmp_lg_u32 s22, 0
	s_cbranch_scc1 .Lgemm_T_loop
	s_waitcnt lgkmcnt(9)
	s_add_u32 m0, s11, 0x1e080
	v_mfma_f32_16x16x32_f16 v[82:85], v[134:137], v[86:89], v[82:85]
	global_load_lds_dwordx4 v[220:221], off offset:-128 sc1
	v_mfma_f32_16x16x32_f16 v[58:61], v[138:141], v[86:89], v[58:61]
	v_mfma_f32_16x16x32_f16 v[14:17], v[142:145], v[86:89], v[14:17]
	v_mfma_f32_16x16x32_f16 v[78:81], v[134:137], v[90:93], v[78:81]
	v_mfma_f32_16x16x32_f16 v[22:25], v[138:141], v[90:93], v[22:25]
	v_mfma_f32_16x16x32_f16 v[30:33], v[142:145], v[90:93], v[30:33]
	s_add_u32 m0, s11, 0x20080
	v_mfma_f32_16x16x32_f16 v[74:77], v[134:137], v[94:97], v[74:77]
	global_load_lds_dwordx4 v[224:225], off offset:-128 sc1
	v_mfma_f32_16x16x32_f16 v[18:21], v[138:141], v[94:97], v[18:21]
	v_mfma_f32_16x16x32_f16 v[26:29], v[142:145], v[94:97], v[26:29]
	v_mfma_f32_16x16x32_f16 v[70:73], v[134:137], v[98:101], v[70:73]
	v_mfma_f32_16x16x32_f16 v[46:49], v[138:141], v[98:101], v[46:49]
	v_mfma_f32_16x16x32_f16 v[240:243], v[142:145], v[98:101], v[240:243]
	s_add_u32 m0, s11, 0x22080
	v_mfma_f32_16x16x32_f16 v[66:69], v[134:137], v[102:105], v[66:69]
	global_load_lds_dwordx4 v[228:229], off offset:-128 sc1
	v_mfma_f32_16x16x32_f16 v[42:45], v[138:141], v[102:105], v[42:45]
	v_mfma_f32_16x16x32_f16 v[236:239], v[142:145], v[102:105], v[236:239]
	v_mfma_f32_16x16x32_f16 v[62:65], v[134:137], v[106:109], v[62:65]
	v_mfma_f32_16x16x32_f16 v[38:41], v[138:141], v[106:109], v[38:41]
	v_mfma_f32_16x16x32_f16 v[34:37], v[142:145], v[106:109], v[34:37]
	s_waitcnt vmcnt(6) lgkmcnt(0)
	s_barrier
	s_add_u32 m0, s11, 0x0
	ds_read_b128 v[134:137], v162 offset:49152
	global_load_lds_dwordx4 v[218:219], off sc1
	v_mfma_f32_16x16x32_f16 v[82:85], v[146:149], v[110:113], v[82:85]
	ds_read_b128 v[138:141], v162 offset:51200
	v_mfma_f32_16x16x32_f16 v[58:61], v[150:153], v[110:113], v[58:61]
	ds_read_b128 v[142:145], v162 offset:53248
	v_mfma_f32_16x16x32_f16 v[14:17], v[154:157], v[110:113], v[14:17]
	ds_read_b128 v[86:89], v158 offset:49152
	v_mfma_f32_16x16x32_f16 v[78:81], v[146:149], v[114:117], v[78:81]
	ds_read_b128 v[90:93], v158 offset:51200
	v_mfma_f32_16x16x32_f16 v[22:25], v[150:153], v[114:117], v[22:25]
	ds_read_b128 v[94:97], v158 offset:53248
	v_mfma_f32_16x16x32_f16 v[30:33], v[154:157], v[114:117], v[30:33]
	s_add_u32 m0, s11, 0x2000
	ds_read_b128 v[98:101], v158 offset:55296
	global_load_lds_dwordx4 v[222:223], off sc1
	v_mfma_f32_16x16x32_f16 v[74:77], v[146:149], v[118:121], v[74:77]
	ds_read_b128 v[102:105], v158 offset:57344
	v_mfma_f32_16x16x32_f16 v[18:21], v[150:153], v[118:121], v[18:21]
	ds_read_b128 v[106:109], v158 offset:59392
	v_mfma_f32_16x16x32_f16 v[26:29], v[154:157], v[118:121], v[26:29]
	ds_read_b128 v[110:113], v160 offset:49152
	v_mfma_f32_16x16x32_f16 v[70:73], v[146:149], v[122:125], v[70:73]
	ds_read_b128 v[114:117], v160 offset:51200
	v_mfma_f32_16x16x32_f16 v[46:49], v[150:153], v[122:125], v[46:49]
	v_mfma_f32_16x16x32_f16 v[240:243], v[154:157], v[122:125], v[240:243]
	s_add_u32 m0, s11, 0x4000
	ds_read_b128 v[118:121], v160 offset:53248
	global_load_lds_dwordx4 v[226:227], off sc1
	v_mfma_f32_16x16x32_f16 v[66:69], v[146:149], v[126:129], v[66:69]
	ds_read_b128 v[122:125], v160 offset:55296
	v_mfma_f32_16x16x32_f16 v[42:45], v[150:153], v[126:129], v[42:45]
	v_mfma_f32_16x16x32_f16 v[236:239], v[154:157], v[126:129], v[236:239]
	ds_read_b128 v[126:129], v160 offset:57344
	v_mfma_f32_16x16x32_f16 v[62:65], v[146:149], v[130:133], v[62:65]
	v_mfma_f32_16x16x32_f16 v[38:41], v[150:153], v[130:133], v[38:41]
	v_mfma_f32_16x16x32_f16 v[34:37], v[154:157], v[130:133], v[34:37]
	ds_read_b128 v[130:133], v160 offset:59392
	ds_read_b128 v[146:149], v164 offset:49152
	ds_read_b128 v[150:153], v164 offset:51200
	ds_read_b128 v[154:157], v164 offset:53248
	s_waitcnt lgkmcnt(9)
	s_add_u32 m0, s11, 0x6000
	v_mfma_f32_16x16x32_f16 v[82:85], v[134:137], v[86:89], v[82:85]
	global_load_lds_dwordx4 v[220:221], off sc1
	v_mfma_f32_16x16x32_f16 v[58:61], v[138:141], v[86:89], v[58:61]
	v_mfma_f32_16x16x32_f16 v[14:17], v[142:145], v[86:89], v[14:17]
	v_mfma_f32_16x16x32_f16 v[78:81], v[134:137], v[90:93], v[78:81]
	v_mfma_f32_16x16x32_f16 v[22:25], v[138:141], v[90:93], v[22:25]
	v_mfma_f32_16x16x32_f16 v[30:33], v[142:145], v[90:93], v[30:33]
	s_add_u32 m0, s11, 0x8000
	v_mfma_f32_16x16x32_f16 v[74:77], v[134:137], v[94:97], v[74:77]
	global_load_lds_dwordx4 v[224:225], off sc1
	v_mfma_f32_16x16x32_f16 v[18:21], v[138:141], v[94:97], v[18:21]
	v_mfma_f32_16x16x32_f16 v[26:29], v[142:145], v[94:97], v[26:29]
	v_mfma_f32_16x16x32_f16 v[70:73], v[134:137], v[98:101], v[70:73]
	v_mfma_f32_16x16x32_f16 v[46:49], v[138:141], v[98:101], v[46:49]
	v_mfma_f32_16x16x32_f16 v[240:243], v[142:145], v[98:101], v[240:243]
	s_add_u32 m0, s11, 0xa000
	v_mfma_f32_16x16x32_f16 v[66:69], v[134:137], v[102:105], v[66:69]
	global_load_lds_dwordx4 v[228:229], off sc1
	v_mfma_f32_16x16x32_f16 v[42:45], v[138:141], v[102:105], v[42:45]
	v_mfma_f32_16x16x32_f16 v[236:239], v[142:145], v[102:105], v[236:239]
	v_mfma_f32_16x16x32_f16 v[62:65], v[134:137], v[106:109], v[62:65]
	v_mfma_f32_16x16x32_f16 v[38:41], v[138:141], v[106:109], v[38:41]
	v_mfma_f32_16x16x32_f16 v[34:37], v[142:145], v[106:109], v[34:37]
	s_waitcnt vmcnt(6) lgkmcnt(0)
	s_barrier
	s_lshl_b32 s26, s17, 2
	s_add_u32 s26, s24, s26
	s_addc_u32 s27, s25, 0
	v_lshlrev_b32_e32 v50, 4, v231
	global_load_dwordx4 v[10:13], v50, s[26:27]
	global_load_dwordx4 v[6:9], v50, s[26:27] offset:64
	global_load_dwordx4 v[2:5], v50, s[26:27] offset:128
	ds_read_b128 v[134:137], v163
	v_mfma_f32_16x16x32_f16 v[82:85], v[146:149], v[110:113], v[82:85]
	ds_read_b128 v[138:141], v163 offset:2048
	v_mfma_f32_16x16x32_f16 v[58:61], v[150:153], v[110:113], v[58:61]
	ds_read_b128 v[142:145], v163 offset:4096
	v_mfma_f32_16x16x32_f16 v[14:17], v[154:157], v[110:113], v[14:17]
	ds_read_b128 v[86:89], v159
	v_mfma_f32_16x16x32_f16 v[78:81], v[146:149], v[114:117], v[78:81]
	ds_read_b128 v[90:93], v159 offset:2048
	v_mfma_f32_16x16x32_f16 v[22:25], v[150:153], v[114:117], v[22:25]
	ds_read_b128 v[94:97], v159 offset:4096
	v_mfma_f32_16x16x32_f16 v[30:33], v[154:157], v[114:117], v[30:33]
	ds_read_b128 v[98:101], v159 offset:6144
	v_mfma_f32_16x16x32_f16 v[74:77], v[146:149], v[118:121], v[74:77]
	ds_read_b128 v[102:105], v159 offset:8192
	v_mfma_f32_16x16x32_f16 v[18:21], v[150:153], v[118:121], v[18:21]
	ds_read_b128 v[106:109], v159 offset:10240
	v_mfma_f32_16x16x32_f16 v[26:29], v[154:157], v[118:121], v[26:29]
	ds_read_b128 v[110:113], v161
	v_mfma_f32_16x16x32_f16 v[70:73], v[146:149], v[122:125], v[70:73]
	ds_read_b128 v[114:117], v161 offset:2048
	v_mfma_f32_16x16x32_f16 v[46:49], v[150:153], v[122:125], v[46:49]
	v_mfma_f32_16x16x32_f16 v[240:243], v[154:157], v[122:125], v[240:243]
	ds_read_b128 v[118:121], v161 offset:4096
	v_mfma_f32_16x16x32_f16 v[66:69], v[146:149], v[126:129], v[66:69]
	ds_read_b128 v[122:125], v161 offset:6144
	v_mfma_f32_16x16x32_f16 v[42:45], v[150:153], v[126:129], v[42:45]
	v_mfma_f32_16x16x32_f16 v[236:239], v[154:157], v[126:129], v[236:239]
	ds_read_b128 v[126:129], v161 offset:8192
	v_mfma_f32_16x16x32_f16 v[62:65], v[146:149], v[130:133], v[62:65]
	v_mfma_f32_16x16x32_f16 v[38:41], v[150:153], v[130:133], v[38:41]
	v_mfma_f32_16x16x32_f16 v[34:37], v[154:157], v[130:133], v[34:37]
	ds_read_b128 v[130:133], v161 offset:10240
	ds_read_b128 v[146:149], v165
	ds_read_b128 v[150:153], v165 offset:2048
	ds_read_b128 v[154:157], v165 offset:4096
	s_waitcnt lgkmcnt(9)
	v_mfma_f32_16x16x32_f16 v[82:85], v[134:137], v[86:89], v[82:85]
	v_mfma_f32_16x16x32_f16 v[58:61], v[138:141], v[86:89], v[58:61]
	v_mfma_f32_16x16x32_f16 v[14:17], v[142:145], v[86:89], v[14:17]
	v_mfma_f32_16x16x32_f16 v[78:81], v[134:137], v[90:93], v[78:81]
	v_mfma_f32_16x16x32_f16 v[22:25], v[138:141], v[90:93], v[22:25]
	v_mfma_f32_16x16x32_f16 v[30:33], v[142:145], v[90:93], v[30:33]
	v_mfma_f32_16x16x32_f16 v[74:77], v[134:137], v[94:97], v[74:77]
	v_mfma_f32_16x16x32_f16 v[18:21], v[138:141], v[94:97], v[18:21]
	v_mfma_f32_16x16x32_f16 v[26:29], v[142:145], v[94:97], v[26:29]
	v_mfma_f32_16x16x32_f16 v[70:73], v[134:137], v[98:101], v[70:73]
	v_mfma_f32_16x16x32_f16 v[46:49], v[138:141], v[98:101], v[46:49]
	v_mfma_f32_16x16x32_f16 v[240:243], v[142:145], v[98:101], v[240:243]
	v_mfma_f32_16x16x32_f16 v[66:69], v[134:137], v[102:105], v[66:69]
	v_mfma_f32_16x16x32_f16 v[42:45], v[138:141], v[102:105], v[42:45]
	v_mfma_f32_16x16x32_f16 v[236:239], v[142:145], v[102:105], v[236:239]
	v_mfma_f32_16x16x32_f16 v[62:65], v[134:137], v[106:109], v[62:65]
	v_mfma_f32_16x16x32_f16 v[38:41], v[138:141], v[106:109], v[38:41]
	v_mfma_f32_16x16x32_f16 v[34:37], v[142:145], v[106:109], v[34:37]
	s_waitcnt vmcnt(3) lgkmcnt(0)
	s_barrier
	ds_read_b128 v[134:137], v162
	v_mfma_f32_16x16x32_f16 v[82:85], v[146:149], v[110:113], v[82:85]
	ds_read_b128 v[138:141], v162 offset:2048
	v_mfma_f32_16x16x32_f16 v[58:61], v[150:153], v[110:113], v[58:61]
	ds_read_b128 v[142:145], v162 offset:4096
	v_mfma_f32_16x16x32_f16 v[14:17], v[154:157], v[110:113], v[14:17]
	ds_read_b128 v[86:89], v158
	v_mfma_f32_16x16x32_f16 v[78:81], v[146:149], v[114:117], v[78:81]
	ds_read_b128 v[90:93], v158 offset:2048
	v_mfma_f32_16x16x32_f16 v[22:25], v[150:153], v[114:117], v[22:25]
	ds_read_b128 v[94:97], v158 offset:4096
	v_mfma_f32_16x16x32_f16 v[30:33], v[154:157], v[114:117], v[30:33]
	ds_read_b128 v[98:101], v158 offset:6144
	v_mfma_f32_16x16x32_f16 v[74:77], v[146:149], v[118:121], v[74:77]
	ds_read_b128 v[102:105], v158 offset:8192
	v_mfma_f32_16x16x32_f16 v[18:21], v[150:153], v[118:121], v[18:21]
	ds_read_b128 v[106:109], v158 offset:10240
	v_mfma_f32_16x16x32_f16 v[26:29], v[154:157], v[118:121], v[26:29]
	ds_read_b128 v[110:113], v160
	v_mfma_f32_16x16x32_f16 v[70:73], v[146:149], v[122:125], v[70:73]
	ds_read_b128 v[114:117], v160 offset:2048
	v_mfma_f32_16x16x32_f16 v[46:49], v[150:153], v[122:125], v[46:49]
	v_mfma_f32_16x16x32_f16 v[240:243], v[154:157], v[122:125], v[240:243]
	ds_read_b128 v[118:121], v160 offset:4096
	v_mfma_f32_16x16x32_f16 v[66:69], v[146:149], v[126:129], v[66:69]
	ds_read_b128 v[122:125], v160 offset:6144
	v_mfma_f32_16x16x32_f16 v[42:45], v[150:153], v[126:129], v[42:45]
	v_mfma_f32_16x16x32_f16 v[236:239], v[154:157], v[126:129], v[236:239]
	ds_read_b128 v[126:129], v160 offset:8192
	v_mfma_f32_16x16x32_f16 v[62:65], v[146:149], v[130:133], v[62:65]
	v_mfma_f32_16x16x32_f16 v[38:41], v[150:153], v[130:133], v[38:41]
	v_mfma_f32_16x16x32_f16 v[34:37], v[154:157], v[130:133], v[34:37]
	ds_read_b128 v[130:133], v160 offset:10240
	ds_read_b128 v[146:149], v164
	ds_read_b128 v[150:153], v164 offset:2048
	ds_read_b128 v[154:157], v164 offset:4096
	s_waitcnt lgkmcnt(9)
	v_mfma_f32_16x16x32_f16 v[82:85], v[134:137], v[86:89], v[82:85]
	v_mfma_f32_16x16x32_f16 v[58:61], v[138:141], v[86:89], v[58:61]
	v_mfma_f32_16x16x32_f16 v[14:17], v[142:145], v[86:89], v[14:17]
	v_mfma_f32_16x16x32_f16 v[78:81], v[134:137], v[90:93], v[78:81]
	v_mfma_f32_16x16x32_f16 v[22:25], v[138:141], v[90:93], v[22:25]
	v_mfma_f32_16x16x32_f16 v[30:33], v[142:145], v[90:93], v[30:33]
	v_mfma_f32_16x16x32_f16 v[74:77], v[134:137], v[94:97], v[74:77]
	v_mfma_f32_16x16x32_f16 v[18:21], v[138:141], v[94:97], v[18:21]
	v_mfma_f32_16x16x32_f16 v[26:29], v[142:145], v[94:97], v[26:29]
	v_mfma_f32_16x16x32_f16 v[70:73], v[134:137], v[98:101], v[70:73]
	v_mfma_f32_16x16x32_f16 v[46:49], v[138:141], v[98:101], v[46:49]
	v_mfma_f32_16x16x32_f16 v[240:243], v[142:145], v[98:101], v[240:243]
	v_mfma_f32_16x16x32_f16 v[66:69], v[134:137], v[102:105], v[66:69]
	v_mfma_f32_16x16x32_f16 v[42:45], v[138:141], v[102:105], v[42:45]
	v_mfma_f32_16x16x32_f16 v[236:239], v[142:145], v[102:105], v[236:239]
	v_mfma_f32_16x16x32_f16 v[62:65], v[134:137], v[106:109], v[62:65]
	v_mfma_f32_16x16x32_f16 v[38:41], v[138:141], v[106:109], v[38:41]
	v_mfma_f32_16x16x32_f16 v[34:37], v[142:145], v[106:109], v[34:37]
	s_waitcnt lgkmcnt(0)
	v_mfma_f32_16x16x32_f16 v[82:85], v[146:149], v[110:113], v[82:85]
	v_mfma_f32_16x16x32_f16 v[58:61], v[150:153], v[110:113], v[58:61]
	v_mfma_f32_16x16x32_f16 v[14:17], v[154:157], v[110:113], v[14:17]
	v_mfma_f32_16x16x32_f16 v[78:81], v[146:149], v[114:117], v[78:81]
	v_mfma_f32_16x16x32_f16 v[22:25], v[150:153], v[114:117], v[22:25]
	v_mfma_f32_16x16x32_f16 v[30:33], v[154:157], v[114:117], v[30:33]
	v_mfma_f32_16x16x32_f16 v[74:77], v[146:149], v[118:121], v[74:77]
	v_mfma_f32_16x16x32_f16 v[18:21], v[150:153], v[118:121], v[18:21]
	v_mfma_f32_16x16x32_f16 v[26:29], v[154:157], v[118:121], v[26:29]
	v_mfma_f32_16x16x32_f16 v[70:73], v[146:149], v[122:125], v[70:73]
	v_mfma_f32_16x16x32_f16 v[46:49], v[150:153], v[122:125], v[46:49]
	v_mfma_f32_16x16x32_f16 v[240:243], v[154:157], v[122:125], v[240:243]
	v_mfma_f32_16x16x32_f16 v[66:69], v[146:149], v[126:129], v[66:69]
	v_mfma_f32_16x16x32_f16 v[42:45], v[150:153], v[126:129], v[42:45]
	v_mfma_f32_16x16x32_f16 v[236:239], v[154:157], v[126:129], v[236:239]
	v_mfma_f32_16x16x32_f16 v[62:65], v[146:149], v[130:133], v[62:65]
	v_mfma_f32_16x16x32_f16 v[38:41], v[150:153], v[130:133], v[38:41]
	v_mfma_f32_16x16x32_f16 v[34:37], v[154:157], v[130:133], v[34:37]
	s_branch .LBB1_76
.Lgemm_N_loop:
	s_waitcnt lgkmcnt(9)
	s_add_u32 m0, s11, 0x1e080
	v_mfma_f32_16x16x32_f16 v[82:85], v[86:89], v[134:137], v[82:85]
	global_load_lds_dwordx4 v[220:221], off offset:-128 sc1
	v_mfma_f32_16x16x32_f16 v[58:61], v[86:89], v[138:141], v[58:61]
	v_mfma_f32_16x16x32_f16 v[14:17], v[86:89], v[142:145], v[14:17]
	v_mfma_f32_16x16x32_f16 v[78:81], v[90:93], v[134:137], v[78:81]
	v_mfma_f32_16x16x32_f16 v[22:25], v[90:93], v[138:141], v[22:25]
	v_mfma_f32_16x16x32_f16 v[30:33], v[90:93], v[142:145], v[30:33]
	s_add_u32 m0, s11, 0x20080
	v_mfma_f32_16x16x32_f16 v[74:77], v[94:97], v[134:137], v[74:77]
	global_load_lds_dwordx4 v[224:225], off offset:-128 sc1
	v_mfma_f32_16x16x32_f16 v[18:21], v[94:97], v[138:141], v[18:21]
	v_mfma_f32_16x16x32_f16 v[26:29], v[94:97], v[142:145], v[26:29]
	v_mfma_f32_16x16x32_f16 v[70:73], v[98:101], v[134:137], v[70:73]
	v_mfma_f32_16x16x32_f16 v[46:49], v[98:101], v[138:141], v[46:49]
	v_mfma_f32_16x16x32_f16 v[240:243], v[98:101], v[142:145], v[240:243]
	s_add_u32 m0, s11, 0x22080
	v_mfma_f32_16x16x32_f16 v[66:69], v[102:105], v[134:137], v[66:69]
	global_load_lds_dwordx4 v[228:229], off offset:-128 sc1
	v_mfma_f32_16x16x32_f16 v[42:45], v[102:105], v[138:141], v[42:45]
	v_mfma_f32_16x16x32_f16 v[236:239], v[102:105], v[142:145], v[236:239]
	v_mfma_f32_16x16x32_f16 v[62:65], v[106:109], v[134:137], v[62:65]
	v_mfma_f32_16x16x32_f16 v[38:41], v[106:109], v[138:141], v[38:41]
	v_mfma_f32_16x16x32_f16 v[34:37], v[106:109], v[142:145], v[34:37]
	s_waitcnt vmcnt(6) lgkmcnt(0)
	s_barrier
	s_add_u32 m0, s11, 0x0
	ds_read_b128 v[134:137], v162 offset:49152
	global_load_lds_dwordx4 v[218:219], off sc1
	v_mfma_f32_16x16x32_f16 v[82:85], v[110:113], v[146:149], v[82:85]
	ds_read_b128 v[138:141], v162 offset:51200
	v_mfma_f32_16x16x32_f16 v[58:61], v[110:113], v[150:153], v[58:61]
	ds_read_b128 v[142:145], v162 offset:53248
	v_mfma_f32_16x16x32_f16 v[14:17], v[110:113], v[154:157], v[14:17]
	ds_read_b128 v[86:89], v158 offset:49152
	v_mfma_f32_16x16x32_f16 v[78:81], v[114:117], v[146:149], v[78:81]
	ds_read_b128 v[90:93], v158 offset:51200
	v_mfma_f32_16x16x32_f16 v[22:25], v[114:117], v[150:153], v[22:25]
	ds_read_b128 v[94:97], v158 offset:53248
	v_mfma_f32_16x16x32_f16 v[30:33], v[114:117], v[154:157], v[30:33]
	s_add_u32 m0, s11, 0x2000
	ds_read_b128 v[98:101], v158 offset:55296
	global_load_lds_dwordx4 v[222:223], off sc1
	v_mfma_f32_16x16x32_f16 v[74:77], v[118:121], v[146:149], v[74:77]
	ds_read_b128 v[102:105], v158 offset:57344
	v_mfma_f32_16x16x32_f16 v[18:21], v[118:121], v[150:153], v[18:21]
	ds_read_b128 v[106:109], v158 offset:59392
	v_mfma_f32_16x16x32_f16 v[26:29], v[118:121], v[154:157], v[26:29]
	ds_read_b128 v[110:113], v160 offset:49152
	v_mfma_f32_16x16x32_f16 v[70:73], v[122:125], v[146:149], v[70:73]
	ds_read_b128 v[114:117], v160 offset:51200
	v_mfma_f32_16x16x32_f16 v[46:49], v[122:125], v[150:153], v[46:49]
	v_mfma_f32_16x16x32_f16 v[240:243], v[122:125], v[154:157], v[240:243]
	s_add_u32 m0, s11, 0x4000
	ds_read_b128 v[118:121], v160 offset:53248
	global_load_lds_dwordx4 v[226:227], off sc1
	v_mfma_f32_16x16x32_f16 v[66:69], v[126:129], v[146:149], v[66:69]
	ds_read_b128 v[122:125], v160 offset:55296
	v_mfma_f32_16x16x32_f16 v[42:45], v[126:129], v[150:153], v[42:45]
	v_mfma_f32_16x16x32_f16 v[236:239], v[126:129], v[154:157], v[236:239]
	ds_read_b128 v[126:129], v160 offset:57344
	v_mfma_f32_16x16x32_f16 v[62:65], v[130:133], v[146:149], v[62:65]
	v_mfma_f32_16x16x32_f16 v[38:41], v[130:133], v[150:153], v[38:41]
	v_mfma_f32_16x16x32_f16 v[34:37], v[130:133], v[154:157], v[34:37]
	ds_read_b128 v[130:133], v160 offset:59392
	ds_read_b128 v[146:149], v164 offset:49152
	ds_read_b128 v[150:153], v164 offset:51200
	ds_read_b128 v[154:157], v164 offset:53248
	s_waitcnt lgkmcnt(9)
	s_add_u32 m0, s11, 0x6000
	v_mfma_f32_16x16x32_f16 v[82:85], v[86:89], v[134:137], v[82:85]
	global_load_lds_dwordx4 v[220:221], off sc1
	v_mfma_f32_16x16x32_f16 v[58:61], v[86:89], v[138:141], v[58:61]
	v_mfma_f32_16x16x32_f16 v[14:17], v[86:89], v[142:145], v[14:17]
	v_mfma_f32_16x16x32_f16 v[78:81], v[90:93], v[134:137], v[78:81]
	v_mfma_f32_16x16x32_f16 v[22:25], v[90:93], v[138:141], v[22:25]
	v_mfma_f32_16x16x32_f16 v[30:33], v[90:93], v[142:145], v[30:33]
	s_add_u32 m0, s11, 0x8000
	v_mfma_f32_16x16x32_f16 v[74:77], v[94:97], v[134:137], v[74:77]
	global_load_lds_dwordx4 v[224:225], off sc1
	v_mfma_f32_16x16x32_f16 v[18:21], v[94:97], v[138:141], v[18:21]
	v_mfma_f32_16x16x32_f16 v[26:29], v[94:97], v[142:145], v[26:29]
	v_mfma_f32_16x16x32_f16 v[70:73], v[98:101], v[134:137], v[70:73]
	v_mfma_f32_16x16x32_f16 v[46:49], v[98:101], v[138:141], v[46:49]
	v_mfma_f32_16x16x32_f16 v[240:243], v[98:101], v[142:145], v[240:243]
	s_add_u32 m0, s11, 0xa000
	v_mfma_f32_16x16x32_f16 v[66:69], v[102:105], v[134:137], v[66:69]
	global_load_lds_dwordx4 v[228:229], off sc1
	v_mfma_f32_16x16x32_f16 v[42:45], v[102:105], v[138:141], v[42:45]
	v_mfma_f32_16x16x32_f16 v[236:239], v[102:105], v[142:145], v[236:239]
	v_mfma_f32_16x16x32_f16 v[62:65], v[106:109], v[134:137], v[62:65]
	v_mfma_f32_16x16x32_f16 v[38:41], v[106:109], v[138:141], v[38:41]
	v_mfma_f32_16x16x32_f16 v[34:37], v[106:109], v[142:145], v[34:37]
	s_waitcnt vmcnt(6) lgkmcnt(0)
	s_barrier
	s_add_u32 m0, s11, 0xbf80
	ds_read_b128 v[134:137], v163
	global_load_lds_dwordx4 v[218:219], off offset:128 sc1
	v_mfma_f32_16x16x32_f16 v[82:85], v[110:113], v[146:149], v[82:85]
	ds_read_b128 v[138:141], v163 offset:2048
	v_mfma_f32_16x16x32_f16 v[58:61], v[110:113], v[150:153], v[58:61]
	ds_read_b128 v[142:145], v163 offset:4096
	v_mfma_f32_16x16x32_f16 v[14:17], v[110:113], v[154:157], v[14:17]
	ds_read_b128 v[86:89], v159
	v_mfma_f32_16x16x32_f16 v[78:81], v[114:117], v[146:149], v[78:81]
	ds_read_b128 v[90:93], v159 offset:2048
	v_mfma_f32_16x16x32_f16 v[22:25], v[114:117], v[150:153], v[22:25]
	ds_read_b128 v[94:97], v159 offset:4096
	v_mfma_f32_16x16x32_f16 v[30:33], v[114:117], v[154:157], v[30:33]
	s_add_u32 m0, s11, 0xdf80
	ds_read_b128 v[98:101], v159 offset:6144
	global_load_lds_dwordx4 v[222:223], off offset:128 sc1
	v_mfma_f32_16x16x32_f16 v[74:77], v[118:121], v[146:149], v[74:77]
	ds_read_b128 v[102:105], v159 offset:8192
	v_mfma_f32_16x16x32_f16 v[18:21], v[118:121], v[150:153], v[18:21]
	ds_read_b128 v[106:109], v159 offset:10240
	v_mfma_f32_16x16x32_f16 v[26:29], v[118:121], v[154:157], v[26:29]
	ds_read_b128 v[110:113], v161
	v_mfma_f32_16x16x32_f16 v[70:73], v[122:125], v[146:149], v[70:73]
	ds_read_b128 v[114:117], v161 offset:2048
	v_mfma_f32_16x16x32_f16 v[46:49], v[122:125], v[150:153], v[46:49]
	v_mfma_f32_16x16x32_f16 v[240:243], v[122:125], v[154:157], v[240:243]
	s_add_u32 m0, s11, 0xff80
	ds_read_b128 v[118:121], v161 offset:4096
	global_load_lds_dwordx4 v[226:227], off offset:128 sc1
	v_mfma_f32_16x16x32_f16 v[66:69], v[126:129], v[146:149], v[66:69]
	ds_read_b128 v[122:125], v161 offset:6144
	v_mfma_f32_16x16x32_f16 v[42:45], v[126:129], v[150:153], v[42:45]
	v_mfma_f32_16x16x32_f16 v[236:239], v[126:129], v[154:157], v[236:239]
	ds_read_b128 v[126:129], v161 offset:8192
	v_mfma_f32_16x16x32_f16 v[62:65], v[130:133], v[146:149], v[62:65]
	v_mfma_f32_16x16x32_f16 v[38:41], v[130:133], v[150:153], v[38:41]
	v_mfma_f32_16x16x32_f16 v[34:37], v[130:133], v[154:157], v[34:37]
	ds_read_b128 v[130:133], v161 offset:10240
	ds_read_b128 v[146:149], v165
	ds_read_b128 v[150:153], v165 offset:2048
	ds_read_b128 v[154:157], v165 offset:4096
	s_waitcnt lgkmcnt(9)
	s_add_u32 m0, s11, 0x11f80
	v_mfma_f32_16x16x32_f16 v[82:85], v[86:89], v[134:137], v[82:85]
	global_load_lds_dwordx4 v[220:221], off offset:128 sc1
	v_mfma_f32_16x16x32_f16 v[58:61], v[86:89], v[138:141], v[58:61]
	v_mfma_f32_16x16x32_f16 v[14:17], v[86:89], v[142:145], v[14:17]
	v_mfma_f32_16x16x32_f16 v[78:81], v[90:93], v[134:137], v[78:81]
	v_mfma_f32_16x16x32_f16 v[22:25], v[90:93], v[138:141], v[22:25]
	v_mfma_f32_16x16x32_f16 v[30:33], v[90:93], v[142:145], v[30:33]
	s_add_u32 m0, s11, 0x13f80
	v_mfma_f32_16x16x32_f16 v[74:77], v[94:97], v[134:137], v[74:77]
	global_load_lds_dwordx4 v[224:225], off offset:128 sc1
	v_mfma_f32_16x16x32_f16 v[18:21], v[94:97], v[138:141], v[18:21]
	v_mfma_f32_16x16x32_f16 v[26:29], v[94:97], v[142:145], v[26:29]
	v_mfma_f32_16x16x32_f16 v[70:73], v[98:101], v[134:137], v[70:73]
	v_mfma_f32_16x16x32_f16 v[46:49], v[98:101], v[138:141], v[46:49]
	v_mfma_f32_16x16x32_f16 v[240:243], v[98:101], v[142:145], v[240:243]
	s_add_u32 m0, s11, 0x15f80
	v_mfma_f32_16x16x32_f16 v[66:69], v[102:105], v[134:137], v[66:69]
	global_load_lds_dwordx4 v[228:229], off offset:128 sc1
	v_mfma_f32_16x16x32_f16 v[42:45], v[102:105], v[138:141], v[42:45]
	v_mfma_f32_16x16x32_f16 v[236:239], v[102:105], v[142:145], v[236:239]
	v_mfma_f32_16x16x32_f16 v[62:65], v[106:109], v[134:137], v[62:65]
	v_mfma_f32_16x16x32_f16 v[38:41], v[106:109], v[138:141], v[38:41]
	v_mfma_f32_16x16x32_f16 v[34:37], v[106:109], v[142:145], v[34:37]
	s_waitcnt vmcnt(6) lgkmcnt(0)
	s_barrier
	s_add_u32 m0, s11, 0x17f00
	ds_read_b128 v[134:137], v162
	global_load_lds_dwordx4 v[218:219], off offset:256 sc1
	v_mfma_f32_16x16x32_f16 v[82:85], v[110:113], v[146:149], v[82:85]
	ds_read_b128 v[138:141], v162 offset:2048
	v_mfma_f32_16x16x32_f16 v[58:61], v[110:113], v[150:153], v[58:61]
	ds_read_b128 v[142:145], v162 offset:4096
	v_mfma_f32_16x16x32_f16 v[14:17], v[110:113], v[154:157], v[14:17]
	ds_read_b128 v[86:89], v158
	v_mfma_f32_16x16x32_f16 v[78:81], v[114:117], v[146:149], v[78:81]
	ds_read_b128 v[90:93], v158 offset:2048
	v_mfma_f32_16x16x32_f16 v[22:25], v[114:117], v[150:153], v[22:25]
	ds_read_b128 v[94:97], v158 offset:4096
	v_mfma_f32_16x16x32_f16 v[30:33], v[114:117], v[154:157], v[30:33]
	s_add_u32 m0, s11, 0x19f00
	ds_read_b128 v[98:101], v158 offset:6144
	global_load_lds_dwordx4 v[222:223], off offset:256 sc1
	v_mfma_f32_16x16x32_f16 v[74:77], v[118:121], v[146:149], v[74:77]
	ds_read_b128 v[102:105], v158 offset:8192
	v_mfma_f32_16x16x32_f16 v[18:21], v[118:121], v[150:153], v[18:21]
	ds_read_b128 v[106:109], v158 offset:10240
	v_mfma_f32_16x16x32_f16 v[26:29], v[118:121], v[154:157], v[26:29]
	ds_read_b128 v[110:113], v160
	v_mfma_f32_16x16x32_f16 v[70:73], v[122:125], v[146:149], v[70:73]
	ds_read_b128 v[114:117], v160 offset:2048
	v_mfma_f32_16x16x32_f16 v[46:49], v[122:125], v[150:153], v[46:49]
	v_mfma_f32_16x16x32_f16 v[240:243], v[122:125], v[154:157], v[240:243]
	s_add_u32 m0, s11, 0x1bf00
	ds_read_b128 v[118:121], v160 offset:4096
	global_load_lds_dwordx4 v[226:227], off offset:256 sc1
	v_mfma_f32_16x16x32_f16 v[66:69], v[126:129], v[146:149], v[66:69]
	ds_read_b128 v[122:125], v160 offset:6144
	v_mfma_f32_16x16x32_f16 v[42:45], v[126:129], v[150:153], v[42:45]
	v_mfma_f32_16x16x32_f16 v[236:239], v[126:129], v[154:157], v[236:239]
	ds_read_b128 v[126:129], v160 offset:8192
	v_mfma_f32_16x16x32_f16 v[62:65], v[130:133], v[146:149], v[62:65]
	v_mfma_f32_16x16x32_f16 v[38:41], v[130:133], v[150:153], v[38:41]
	v_mfma_f32_16x16x32_f16 v[34:37], v[130:133], v[154:157], v[34:37]
	ds_read_b128 v[130:133], v160 offset:10240
	ds_read_b128 v[146:149], v164
	ds_read_b128 v[150:153], v164 offset:2048
	ds_read_b128 v[154:157], v164 offset:4096
	v_lshl_add_u64 v[218:219], v[218:219], 0, s[20:21]
	v_lshl_add_u64 v[222:223], v[222:223], 0, s[20:21]
	v_lshl_add_u64 v[226:227], v[226:227], 0, s[20:21]
	v_lshl_add_u64 v[220:221], v[220:221], 0, s[20:21]
	v_lshl_add_u64 v[224:225], v[224:225], 0, s[20:21]
	v_lshl_add_u64 v[228:229], v[228:229], 0, s[20:21]
	s_sub_u32 s22, s22, 1
	s_cmp_lg_u32 s22, 0
	s_cbranch_scc1 .Lgemm_N_loop
	s_waitcnt lgkmcnt(9)
	s_add_u32 m0, s11, 0x1e080
	v_mfma_f32_16x16x32_f16 v[82:85], v[86:89], v[134:137], v[82:85]
	global_load_lds_dwordx4 v[220:221], off offset:-128 sc1
	v_mfma_f32_16x16x32_f16 v[58:61], v[86:89], v[138:141], v[58:61]
	v_mfma_f32_16x16x32_f16 v[14:17], v[86:89], v[142:145], v[14:17]
	v_mfma_f32_16x16x32_f16 v[78:81], v[90:93], v[134:137], v[78:81]
	v_mfma_f32_16x16x32_f16 v[22:25], v[90:93], v[138:141], v[22:25]
	v_mfma_f32_16x16x32_f16 v[30:33], v[90:93], v[142:145], v[30:33]
	s_add_u32 m0, s11, 0x20080
	v_mfma_f32_16x16x32_f16 v[74:77], v[94:97], v[134:137], v[74:77]
	global_load_lds_dwordx4 v[224:225], off offset:-128 sc1
	v_mfma_f32_16x16x32_f16 v[18:21], v[94:97], v[138:141], v[18:21]
	v_mfma_f32_16x16x32_f16 v[26:29], v[94:97], v[142:145], v[26:29]
	v_mfma_f32_16x16x32_f16 v[70:73], v[98:101], v[134:137], v[70:73]
	v_mfma_f32_16x16x32_f16 v[46:49], v[98:101], v[138:141], v[46:49]
	v_mfma_f32_16x16x32_f16 v[240:243], v[98:101], v[142:145], v[240:243]
	s_add_u32 m0, s11, 0x22080
	v_mfma_f32_16x16x32_f16 v[66:69], v[102:105], v[134:137], v[66:69]
	global_load_lds_dwordx4 v[228:229], off offset:-128 sc1
	v_mfma_f32_16x16x32_f16 v[42:45], v[102:105], v[138:141], v[42:45]
	v_mfma_f32_16x16x32_f16 v[236:239], v[102:105], v[142:145], v[236:239]
	v_mfma_f32_16x16x32_f16 v[62:65], v[106:109], v[134:137], v[62:65]
	v_mfma_f32_16x16x32_f16 v[38:41], v[106:109], v[138:141], v[38:41]
	v_mfma_f32_16x16x32_f16 v[34:37], v[106:109], v[142:145], v[34:37]
	s_waitcnt vmcnt(6) lgkmcnt(0)
	s_barrier
	s_add_u32 m0, s11, 0x0
	ds_read_b128 v[134:137], v162 offset:49152
	global_load_lds_dwordx4 v[218:219], off sc1
	v_mfma_f32_16x16x32_f16 v[82:85], v[110:113], v[146:149], v[82:85]
	ds_read_b128 v[138:141], v162 offset:51200
	v_mfma_f32_16x16x32_f16 v[58:61], v[110:113], v[150:153], v[58:61]
	ds_read_b128 v[142:145], v162 offset:53248
	v_mfma_f32_16x16x32_f16 v[14:17], v[110:113], v[154:157], v[14:17]
	ds_read_b128 v[86:89], v158 offset:49152
	v_mfma_f32_16x16x32_f16 v[78:81], v[114:117], v[146:149], v[78:81]
	ds_read_b128 v[90:93], v158 offset:51200
	v_mfma_f32_16x16x32_f16 v[22:25], v[114:117], v[150:153], v[22:25]
	ds_read_b128 v[94:97], v158 offset:53248
	v_mfma_f32_16x16x32_f16 v[30:33], v[114:117], v[154:157], v[30:33]
	s_add_u32 m0, s11, 0x2000
	ds_read_b128 v[98:101], v158 offset:55296
	global_load_lds_dwordx4 v[222:223], off sc1
	v_mfma_f32_16x16x32_f16 v[74:77], v[118:121], v[146:149], v[74:77]
	ds_read_b128 v[102:105], v158 offset:57344
	v_mfma_f32_16x16x32_f16 v[18:21], v[118:121], v[150:153], v[18:21]
	ds_read_b128 v[106:109], v158 offset:59392
	v_mfma_f32_16x16x32_f16 v[26:29], v[118:121], v[154:157], v[26:29]
	ds_read_b128 v[110:113], v160 offset:49152
	v_mfma_f32_16x16x32_f16 v[70:73], v[122:125], v[146:149], v[70:73]
	ds_read_b128 v[114:117], v160 offset:51200
	v_mfma_f32_16x16x32_f16 v[46:49], v[122:125], v[150:153], v[46:49]
	v_mfma_f32_16x16x32_f16 v[240:243], v[122:125], v[154:157], v[240:243]
	s_add_u32 m0, s11, 0x4000
	ds_read_b128 v[118:121], v160 offset:53248
	global_load_lds_dwordx4 v[226:227], off sc1
	v_mfma_f32_16x16x32_f16 v[66:69], v[126:129], v[146:149], v[66:69]
	ds_read_b128 v[122:125], v160 offset:55296
	v_mfma_f32_16x16x32_f16 v[42:45], v[126:129], v[150:153], v[42:45]
	v_mfma_f32_16x16x32_f16 v[236:239], v[126:129], v[154:157], v[236:239]
	ds_read_b128 v[126:129], v160 offset:57344
	v_mfma_f32_16x16x32_f16 v[62:65], v[130:133], v[146:149], v[62:65]
	v_mfma_f32_16x16x32_f16 v[38:41], v[130:133], v[150:153], v[38:41]
	v_mfma_f32_16x16x32_f16 v[34:37], v[130:133], v[154:157], v[34:37]
	ds_read_b128 v[130:133], v160 offset:59392
	ds_read_b128 v[146:149], v164 offset:49152
	ds_read_b128 v[150:153], v164 offset:51200
	ds_read_b128 v[154:157], v164 offset:53248
	s_waitcnt lgkmcnt(9)
	s_add_u32 m0, s11, 0x6000
	v_mfma_f32_16x16x32_f16 v[82:85], v[86:89], v[134:137], v[82:85]
	global_load_lds_dwordx4 v[220:221], off sc1
	v_mfma_f32_16x16x32_f16 v[58:61], v[86:89], v[138:141], v[58:61]
	v_mfma_f32_16x16x32_f16 v[14:17], v[86:89], v[142:145], v[14:17]
	v_mfma_f32_16x16x32_f16 v[78:81], v[90:93], v[134:137], v[78:81]
	v_mfma_f32_16x16x32_f16 v[22:25], v[90:93], v[138:141], v[22:25]
	v_mfma_f32_16x16x32_f16 v[30:33], v[90:93], v[142:145], v[30:33]
	s_add_u32 m0, s11, 0x8000
	v_mfma_f32_16x16x32_f16 v[74:77], v[94:97], v[134:137], v[74:77]
	global_load_lds_dwordx4 v[224:225], off sc1
	v_mfma_f32_16x16x32_f16 v[18:21], v[94:97], v[138:141], v[18:21]
	v_mfma_f32_16x16x32_f16 v[26:29], v[94:97], v[142:145], v[26:29]
	v_mfma_f32_16x16x32_f16 v[70:73], v[98:101], v[134:137], v[70:73]
	v_mfma_f32_16x16x32_f16 v[46:49], v[98:101], v[138:141], v[46:49]
	v_mfma_f32_16x16x32_f16 v[240:243], v[98:101], v[142:145], v[240:243]
	s_add_u32 m0, s11, 0xa000
	v_mfma_f32_16x16x32_f16 v[66:69], v[102:105], v[134:137], v[66:69]
	global_load_lds_dwordx4 v[228:229], off sc1
	v_mfma_f32_16x16x32_f16 v[42:45], v[102:105], v[138:141], v[42:45]
	v_mfma_f32_16x16x32_f16 v[236:239], v[102:105], v[142:145], v[236:239]
	v_mfma_f32_16x16x32_f16 v[62:65], v[106:109], v[134:137], v[62:65]
	v_mfma_f32_16x16x32_f16 v[38:41], v[106:109], v[138:141], v[38:41]
	v_mfma_f32_16x16x32_f16 v[34:37], v[106:109], v[142:145], v[34:37]
	s_waitcnt vmcnt(6) lgkmcnt(0)
	s_barrier
	s_lshl_b32 s26, s17, 2
	s_add_u32 s26, s24, s26
	s_addc_u32 s27, s25, 0
	v_lshlrev_b32_e32 v50, 2, v1
	global_load_dword v234, v50, s[26:27]
	global_load_dword v232, v50, s[26:27] offset:64
	global_load_dword v230, v50, s[26:27] offset:128
	ds_read_b128 v[134:137], v163
	v_mfma_f32_16x16x32_f16 v[82:85], v[110:113], v[146:149], v[82:85]
	ds_read_b128 v[138:141], v163 offset:2048
	v_mfma_f32_16x16x32_f16 v[58:61], v[110:113], v[150:153], v[58:61]
	ds_read_b128 v[142:145], v163 offset:4096
	v_mfma_f32_16x16x32_f16 v[14:17], v[110:113], v[154:157], v[14:17]
	ds_read_b128 v[86:89], v159
	v_mfma_f32_16x16x32_f16 v[78:81], v[114:117], v[146:149], v[78:81]
	ds_read_b128 v[90:93], v159 offset:2048
	v_mfma_f32_16x16x32_f16 v[22:25], v[114:117], v[150:153], v[22:25]
	ds_read_b128 v[94:97], v159 offset:4096
	v_mfma_f32_16x16x32_f16 v[30:33], v[114:117], v[154:157], v[30:33]
	ds_read_b128 v[98:101], v159 offset:6144
	v_mfma_f32_16x16x32_f16 v[74:77], v[118:121], v[146:149], v[74:77]
	ds_read_b128 v[102:105], v159 offset:8192
	v_mfma_f32_16x16x32_f16 v[18:21], v[118:121], v[150:153], v[18:21]
	ds_read_b128 v[106:109], v159 offset:10240
	v_mfma_f32_16x16x32_f16 v[26:29], v[118:121], v[154:157], v[26:29]
	ds_read_b128 v[110:113], v161
	v_mfma_f32_16x16x32_f16 v[70:73], v[122:125], v[146:149], v[70:73]
	ds_read_b128 v[114:117], v161 offset:2048
	v_mfma_f32_16x16x32_f16 v[46:49], v[122:125], v[150:153], v[46:49]
	v_mfma_f32_16x16x32_f16 v[240:243], v[122:125], v[154:157], v[240:243]
	ds_read_b128 v[118:121], v161 offset:4096
	v_mfma_f32_16x16x32_f16 v[66:69], v[126:129], v[146:149], v[66:69]
	ds_read_b128 v[122:125], v161 offset:6144
	v_mfma_f32_16x16x32_f16 v[42:45], v[126:129], v[150:153], v[42:45]
	v_mfma_f32_16x16x32_f16 v[236:239], v[126:129], v[154:157], v[236:239]
	ds_read_b128 v[126:129], v161 offset:8192
	v_mfma_f32_16x16x32_f16 v[62:65], v[130:133], v[146:149], v[62:65]
	v_mfma_f32_16x16x32_f16 v[38:41], v[130:133], v[150:153], v[38:41]
	v_mfma_f32_16x16x32_f16 v[34:37], v[130:133], v[154:157], v[34:37]
	ds_read_b128 v[130:133], v161 offset:10240
	ds_read_b128 v[146:149], v165
	ds_read_b128 v[150:153], v165 offset:2048
	ds_read_b128 v[154:157], v165 offset:4096
	s_waitcnt lgkmcnt(9)
	v_mfma_f32_16x16x32_f16 v[82:85], v[86:89], v[134:137], v[82:85]
	v_mfma_f32_16x16x32_f16 v[58:61], v[86:89], v[138:141], v[58:61]
	v_mfma_f32_16x16x32_f16 v[14:17], v[86:89], v[142:145], v[14:17]
	v_mfma_f32_16x16x32_f16 v[78:81], v[90:93], v[134:137], v[78:81]
	v_mfma_f32_16x16x32_f16 v[22:25], v[90:93], v[138:141], v[22:25]
	v_mfma_f32_16x16x32_f16 v[30:33], v[90:93], v[142:145], v[30:33]
	v_mfma_f32_16x16x32_f16 v[74:77], v[94:97], v[134:137], v[74:77]
	v_mfma_f32_16x16x32_f16 v[18:21], v[94:97], v[138:141], v[18:21]
	v_mfma_f32_16x16x32_f16 v[26:29], v[94:97], v[142:145], v[26:29]
	v_mfma_f32_16x16x32_f16 v[70:73], v[98:101], v[134:137], v[70:73]
	v_mfma_f32_16x16x32_f16 v[46:49], v[98:101], v[138:141], v[46:49]
	v_mfma_f32_16x16x32_f16 v[240:243], v[98:101], v[142:145], v[240:243]
	v_mfma_f32_16x16x32_f16 v[66:69], v[102:105], v[134:137], v[66:69]
	v_mfma_f32_16x16x32_f16 v[42:45], v[102:105], v[138:141], v[42:45]
	v_mfma_f32_16x16x32_f16 v[236:239], v[102:105], v[142:145], v[236:239]
	v_mfma_f32_16x16x32_f16 v[62:65], v[106:109], v[134:137], v[62:65]
	v_mfma_f32_16x16x32_f16 v[38:41], v[106:109], v[138:141], v[38:41]
	v_mfma_f32_16x16x32_f16 v[34:37], v[106:109], v[142:145], v[34:37]
	s_waitcnt vmcnt(3) lgkmcnt(0)
	s_barrier
	ds_read_b128 v[134:137], v162
	v_mfma_f32_16x16x32_f16 v[82:85], v[110:113], v[146:149], v[82:85]
	ds_read_b128 v[138:141], v162 offset:2048
	v_mfma_f32_16x16x32_f16 v[58:61], v[110:113], v[150:153], v[58:61]
	ds_read_b128 v[142:145], v162 offset:4096
	v_mfma_f32_16x16x32_f16 v[14:17], v[110:113], v[154:157], v[14:17]
	ds_read_b128 v[86:89], v158
	v_mfma_f32_16x16x32_f16 v[78:81], v[114:117], v[146:149], v[78:81]
	ds_read_b128 v[90:93], v158 offset:2048
	v_mfma_f32_16x16x32_f16 v[22:25], v[114:117], v[150:153], v[22:25]
	ds_read_b128 v[94:97], v158 offset:4096
	v_mfma_f32_16x16x32_f16 v[30:33], v[114:117], v[154:157], v[30:33]
	ds_read_b128 v[98:101], v158 offset:6144
	v_mfma_f32_16x16x32_f16 v[74:77], v[118:121], v[146:149], v[74:77]
	ds_read_b128 v[102:105], v158 offset:8192
	v_mfma_f32_16x16x32_f16 v[18:21], v[118:121], v[150:153], v[18:21]
	ds_read_b128 v[106:109], v158 offset:10240
	v_mfma_f32_16x16x32_f16 v[26:29], v[118:121], v[154:157], v[26:29]
	ds_read_b128 v[110:113], v160
	v_mfma_f32_16x16x32_f16 v[70:73], v[122:125], v[146:149], v[70:73]
	ds_read_b128 v[114:117], v160 offset:2048
	v_mfma_f32_16x16x32_f16 v[46:49], v[122:125], v[150:153], v[46:49]
	v_mfma_f32_16x16x32_f16 v[240:243], v[122:125], v[154:157], v[240:243]
	ds_read_b128 v[118:121], v160 offset:4096
	v_mfma_f32_16x16x32_f16 v[66:69], v[126:129], v[146:149], v[66:69]
	ds_read_b128 v[122:125], v160 offset:6144
	v_mfma_f32_16x16x32_f16 v[42:45], v[126:129], v[150:153], v[42:45]
	v_mfma_f32_16x16x32_f16 v[236:239], v[126:129], v[154:157], v[236:239]
	ds_read_b128 v[126:129], v160 offset:8192
	v_mfma_f32_16x16x32_f16 v[62:65], v[130:133], v[146:149], v[62:65]
	v_mfma_f32_16x16x32_f16 v[38:41], v[130:133], v[150:153], v[38:41]
	v_mfma_f32_16x16x32_f16 v[34:37], v[130:133], v[154:157], v[34:37]
	ds_read_b128 v[130:133], v160 offset:10240
	ds_read_b128 v[146:149], v164
	ds_read_b128 v[150:153], v164 offset:2048
	ds_read_b128 v[154:157], v164 offset:4096
	s_waitcnt lgkmcnt(9)
	v_mfma_f32_16x16x32_f16 v[82:85], v[86:89], v[134:137], v[82:85]
	v_mfma_f32_16x16x32_f16 v[58:61], v[86:89], v[138:141], v[58:61]
	v_mfma_f32_16x16x32_f16 v[14:17], v[86:89], v[142:145], v[14:17]
	v_mfma_f32_16x16x32_f16 v[78:81], v[90:93], v[134:137], v[78:81]
	v_mfma_f32_16x16x32_f16 v[22:25], v[90:93], v[138:141], v[22:25]
	v_mfma_f32_16x16x32_f16 v[30:33], v[90:93], v[142:145], v[30:33]
	v_mfma_f32_16x16x32_f16 v[74:77], v[94:97], v[134:137], v[74:77]
	v_mfma_f32_16x16x32_f16 v[18:21], v[94:97], v[138:141], v[18:21]
	v_mfma_f32_16x16x32_f16 v[26:29], v[94:97], v[142:145], v[26:29]
	v_mfma_f32_16x16x32_f16 v[70:73], v[98:101], v[134:137], v[70:73]
	v_mfma_f32_16x16x32_f16 v[46:49], v[98:101], v[138:141], v[46:49]
	v_mfma_f32_16x16x32_f16 v[240:243], v[98:101], v[142:145], v[240:243]
	v_mfma_f32_16x16x32_f16 v[66:69], v[102:105], v[134:137], v[66:69]
	v_mfma_f32_16x16x32_f16 v[42:45], v[102:105], v[138:141], v[42:45]
	v_mfma_f32_16x16x32_f16 v[236:239], v[102:105], v[142:145], v[236:239]
	v_mfma_f32_16x16x32_f16 v[62:65], v[106:109], v[134:137], v[62:65]
	v_mfma_f32_16x16x32_f16 v[38:41], v[106:109], v[138:141], v[38:41]
	v_mfma_f32_16x16x32_f16 v[34:37], v[106:109], v[142:145], v[34:37]
	s_waitcnt lgkmcnt(0)
	v_mfma_f32_16x16x32_f16 v[82:85], v[110:113], v[146:149], v[82:85]
	v_mfma_f32_16x16x32_f16 v[58:61], v[110:113], v[150:153], v[58:61]
	v_mfma_f32_16x16x32_f16 v[14:17], v[110:113], v[154:157], v[14:17]
	v_mfma_f32_16x16x32_f16 v[78:81], v[114:117], v[146:149], v[78:81]
	v_mfma_f32_16x16x32_f16 v[22:25], v[114:117], v[150:153], v[22:25]
	v_mfma_f32_16x16x32_f16 v[30:33], v[114:117], v[154:157], v[30:33]
	v_mfma_f32_16x16x32_f16 v[74:77], v[118:121], v[146:149], v[74:77]
	v_mfma_f32_16x16x32_f16 v[18:21], v[118:121], v[150:153], v[18:21]
	v_mfma_f32_16x16x32_f16 v[26:29], v[118:121], v[154:157], v[26:29]
	v_mfma_f32_16x16x32_f16 v[70:73], v[122:125], v[146:149], v[70:73]
	v_mfma_f32_16x16x32_f16 v[46:49], v[122:125], v[150:153], v[46:49]
	v_mfma_f32_16x16x32_f16 v[240:243], v[122:125], v[154:157], v[240:243]
	v_mfma_f32_16x16x32_f16 v[66:69], v[126:129], v[146:149], v[66:69]
	v_mfma_f32_16x16x32_f16 v[42:45], v[126:129], v[150:153], v[42:45]
	v_mfma_f32_16x16x32_f16 v[236:239], v[126:129], v[154:157], v[236:239]
	v_mfma_f32_16x16x32_f16 v[62:65], v[130:133], v[146:149], v[62:65]
	v_mfma_f32_16x16x32_f16 v[38:41], v[130:133], v[150:153], v[38:41]
	v_mfma_f32_16x16x32_f16 v[34:37], v[130:133], v[154:157], v[34:37]
